# speedup vs baseline: 1.0072x; 1.0072x over previous
.Lmk_vb:
	s_mov_b32 m0, s13
	s_nop 0
	global_load_lds_dwordx4 v124, s[10:11]
	global_load_dwordx4 v[96:99], v124, s[18:19]
	global_load_dwordx2 v[100:101], v125, s[22:23]
	global_load_dwordx4 v[102:105], v124, s[18:19] offset:1024
	global_load_dwordx2 v[106:107], v125, s[22:23] offset:512
	global_load_dwordx4 v[108:111], v124, s[18:19] offset:2048
	global_load_dwordx2 v[112:113], v125, s[22:23] offset:1024
	global_load_dwordx4 v[114:117], v124, s[18:19] offset:3072
	global_load_dwordx2 v[118:119], v125, s[22:23] offset:1536
	s_add_u32 s24, s10, 0x3000
	s_addc_u32 s25, s11, 0
	s_add_u32 s26, s13, 0x3000
	s_mov_b32 m0, s26
	s_nop 0
	global_load_lds_dwordx4 v124, s[24:25]
	s_add_u32 s24, s10, 0x6000
	s_addc_u32 s25, s11, 0
	s_add_u32 s26, s13, 0x6000
	s_mov_b32 m0, s26
	s_nop 0
	global_load_lds_dwordx4 v124, s[24:25]
	s_add_u32 s24, s10, 0x9000
	s_addc_u32 s25, s11, 0
	s_add_u32 s26, s13, 0x9000
	s_mov_b32 m0, s26
	s_nop 0
	global_load_lds_dwordx4 v124, s[24:25]
	s_add_u32 s24, s10, 0xc000
	s_addc_u32 s25, s11, 0
	s_add_u32 s26, s13, 0xc000
	s_mov_b32 m0, s26
	s_nop 0
	global_load_lds_dwordx4 v124, s[24:25]
	s_waitcnt vmcnt(4)
	s_barrier
	ds_read_b128 v[0:3], v124
	ds_read_b64 v[4:5], v125 offset:4096
	ds_read_b128 v[6:9], v124 offset:1024
	ds_read_b64 v[10:11], v125 offset:4608
	ds_read_b128 v[12:15], v124 offset:2048
	ds_read_b64 v[16:17], v125 offset:5120
	ds_read_b128 v[18:21], v124 offset:3072
	ds_read_b64 v[22:23], v125 offset:5632
	s_waitcnt lgkmcnt(0)
	s_setprio 3
	v_mfma_f32_32x32x64_f8f6f4 v[48:63], v[0:5], v[96:101], 0 cbsz:2 blgp:2
	ds_read_b128 v[24:27], v124 offset:6144
	ds_read_b64 v[28:29], v125 offset:10240
	v_mfma_f32_32x32x64_f8f6f4 v[48:63], v[6:11], v[102:107], v[48:63] cbsz:2 blgp:2
	ds_read_b128 v[30:33], v124 offset:7168
	ds_read_b64 v[34:35], v125 offset:10752
	v_mfma_f32_32x32x64_f8f6f4 v[48:63], v[12:17], v[108:113], v[48:63] cbsz:2 blgp:2
	ds_read_b128 v[36:39], v124 offset:8192
	ds_read_b64 v[40:41], v125 offset:11264
	v_mfma_f32_32x32x64_f8f6f4 v[48:63], v[18:23], v[114:119], v[48:63] cbsz:2 blgp:2
	ds_read_b128 v[42:45], v124 offset:9216
	ds_read_b64 v[46:47], v125 offset:11776
	s_waitcnt vmcnt(3) lgkmcnt(0)
	v_mfma_f32_32x32x64_f8f6f4 v[64:79], v[24:29], v[96:101], 0 cbsz:2 blgp:2
	s_barrier
	s_add_u32 s24, s10, 0xf000
	s_addc_u32 s25, s11, 0
	s_mov_b32 m0, s13
	s_nop 0
	global_load_lds_dwordx4 v124, s[24:25]
	ds_read_b128 v[0:3], v124 offset:12288
	ds_read_b64 v[4:5], v125 offset:16384
	ds_read_b128 v[6:9], v124 offset:13312
	ds_read_b64 v[10:11], v125 offset:16896
	ds_read_b128 v[24:27], v124 offset:18432
	ds_read_b64 v[28:29], v125 offset:22528
	v_mfma_f32_32x32x64_f8f6f4 v[64:79], v[30:35], v[102:107], v[64:79] cbsz:2 blgp:2
	ds_read_b128 v[12:15], v124 offset:14336
	ds_read_b64 v[16:17], v125 offset:17408
	ds_read_b128 v[18:21], v124 offset:15360
	ds_read_b64 v[22:23], v125 offset:17920
	ds_read_b128 v[30:33], v124 offset:19456
	ds_read_b64 v[34:35], v125 offset:23040
	v_exp_f32_e32 v48, v48
	v_exp_f32_e32 v49, v49
	v_exp_f32_e32 v50, v50
	v_exp_f32_e32 v51, v51
	v_mfma_f32_32x32x64_f8f6f4 v[64:79], v[36:41], v[108:113], v[64:79] cbsz:2 blgp:2
	ds_read_b128 v[36:39], v124 offset:20480
	ds_read_b64 v[40:41], v125 offset:23552
	v_exp_f32_e32 v52, v52
	v_exp_f32_e32 v53, v53
	v_exp_f32_e32 v54, v54
	v_exp_f32_e32 v55, v55
	v_pk_add_f32 v[120:121], v[120:121], v[48:49]
	v_pk_add_f32 v[122:123], v[122:123], v[50:51]
	v_mfma_f32_32x32x64_f8f6f4 v[64:79], v[42:47], v[114:119], v[64:79] cbsz:2 blgp:2
	ds_read_b128 v[42:45], v124 offset:21504
	ds_read_b64 v[46:47], v125 offset:24064
	v_exp_f32_e32 v56, v56
	v_exp_f32_e32 v57, v57
	v_exp_f32_e32 v58, v58
	v_exp_f32_e32 v59, v59
	v_pk_add_f32 v[120:121], v[120:121], v[52:53]
	v_pk_add_f32 v[122:123], v[122:123], v[54:55]
	s_waitcnt vmcnt(3) lgkmcnt(6)
	v_mfma_f32_32x32x64_f8f6f4 v[80:95], v[0:5], v[96:101], 0 cbsz:2 blgp:2
	s_barrier
	ds_read_b128 v[0:3], v124 offset:24576
	ds_read_b64 v[4:5], v125 offset:28672
	v_exp_f32_e32 v60, v60
	v_exp_f32_e32 v61, v61
	v_exp_f32_e32 v62, v62
	v_exp_f32_e32 v63, v63
	v_pk_add_f32 v[120:121], v[120:121], v[56:57]
	v_pk_add_f32 v[122:123], v[122:123], v[58:59]
	v_mfma_f32_32x32x64_f8f6f4 v[80:95], v[6:11], v[102:107], v[80:95] cbsz:2 blgp:2
	ds_read_b128 v[6:9], v124 offset:25600
	ds_read_b64 v[10:11], v125 offset:29184
	v_exp_f32_e32 v64, v64
	v_exp_f32_e32 v65, v65
	v_exp_f32_e32 v66, v66
	v_exp_f32_e32 v67, v67
	v_pk_add_f32 v[120:121], v[120:121], v[60:61]
	v_pk_add_f32 v[122:123], v[122:123], v[62:63]
	v_mfma_f32_32x32x64_f8f6f4 v[80:95], v[12:17], v[108:113], v[80:95] cbsz:2 blgp:2
	ds_read_b128 v[12:15], v124 offset:26624
	ds_read_b64 v[16:17], v125 offset:29696
	v_exp_f32_e32 v68, v68
	v_exp_f32_e32 v69, v69
	v_exp_f32_e32 v70, v70
	v_exp_f32_e32 v71, v71
	v_pk_add_f32 v[120:121], v[120:121], v[64:65]
	v_pk_add_f32 v[122:123], v[122:123], v[66:67]
	v_mfma_f32_32x32x64_f8f6f4 v[80:95], v[18:23], v[114:119], v[80:95] cbsz:2 blgp:2
	ds_read_b128 v[18:21], v124 offset:27648
	ds_read_b64 v[22:23], v125 offset:30208
	v_exp_f32_e32 v72, v72
	v_exp_f32_e32 v73, v73
	v_exp_f32_e32 v74, v74
	v_exp_f32_e32 v75, v75
	v_pk_add_f32 v[120:121], v[120:121], v[68:69]
	v_pk_add_f32 v[122:123], v[122:123], v[70:71]
	s_waitcnt lgkmcnt(8)
	v_mfma_f32_32x32x64_f8f6f4 v[48:63], v[24:29], v[96:101], 0 cbsz:2 blgp:2
	ds_read_b128 v[24:27], v124 offset:30720
	ds_read_b64 v[28:29], v125 offset:34816
	v_exp_f32_e32 v76, v76
	v_exp_f32_e32 v77, v77
	v_exp_f32_e32 v78, v78
	v_exp_f32_e32 v79, v79
	v_pk_add_f32 v[120:121], v[120:121], v[72:73]
	v_pk_add_f32 v[122:123], v[122:123], v[74:75]
	v_mfma_f32_32x32x64_f8f6f4 v[48:63], v[30:35], v[102:107], v[48:63] cbsz:2 blgp:2
	ds_read_b128 v[30:33], v124 offset:31744
	ds_read_b64 v[34:35], v125 offset:35328
	v_exp_f32_e32 v80, v80
	v_exp_f32_e32 v81, v81
	v_exp_f32_e32 v82, v82
	v_exp_f32_e32 v83, v83
	v_pk_add_f32 v[120:121], v[120:121], v[76:77]
	v_pk_add_f32 v[122:123], v[122:123], v[78:79]
	v_mfma_f32_32x32x64_f8f6f4 v[48:63], v[36:41], v[108:113], v[48:63] cbsz:2 blgp:2
	ds_read_b128 v[36:39], v124 offset:32768
	ds_read_b64 v[40:41], v125 offset:35840
	v_exp_f32_e32 v84, v84
	v_exp_f32_e32 v85, v85
	v_exp_f32_e32 v86, v86
	v_exp_f32_e32 v87, v87
	v_pk_add_f32 v[120:121], v[120:121], v[80:81]
	v_pk_add_f32 v[122:123], v[122:123], v[82:83]
	v_mfma_f32_32x32x64_f8f6f4 v[48:63], v[42:47], v[114:119], v[48:63] cbsz:2 blgp:2
	ds_read_b128 v[42:45], v124 offset:33792
	ds_read_b64 v[46:47], v125 offset:36352
	v_exp_f32_e32 v88, v88
	v_exp_f32_e32 v89, v89
	v_exp_f32_e32 v90, v90
	v_exp_f32_e32 v91, v91
	v_pk_add_f32 v[120:121], v[120:121], v[84:85]
	v_pk_add_f32 v[122:123], v[122:123], v[86:87]
	s_setprio 2
	s_waitcnt vmcnt(2) lgkmcnt(8)
	v_mfma_f32_32x32x64_f8f6f4 v[64:79], v[0:5], v[96:101], 0 cbsz:2 blgp:2
	s_barrier
	ds_read_b128 v[0:3], v124 offset:36864
	ds_read_b64 v[4:5], v125 offset:40960
	v_exp_f32_e32 v92, v92
	v_exp_f32_e32 v93, v93
	v_exp_f32_e32 v94, v94
	v_exp_f32_e32 v95, v95
	v_pk_add_f32 v[120:121], v[120:121], v[88:89]
	v_pk_add_f32 v[122:123], v[122:123], v[90:91]
	v_mfma_f32_32x32x64_f8f6f4 v[64:79], v[6:11], v[102:107], v[64:79] cbsz:2 blgp:2
	ds_read_b128 v[6:9], v124 offset:37888
	ds_read_b64 v[10:11], v125 offset:41472
	v_exp_f32_e32 v48, v48
	v_exp_f32_e32 v49, v49
	v_exp_f32_e32 v50, v50
	v_exp_f32_e32 v51, v51
	v_pk_add_f32 v[120:121], v[120:121], v[92:93]
	v_pk_add_f32 v[122:123], v[122:123], v[94:95]
	v_mfma_f32_32x32x64_f8f6f4 v[64:79], v[12:17], v[108:113], v[64:79] cbsz:2 blgp:2
	ds_read_b128 v[12:15], v124 offset:38912
	ds_read_b64 v[16:17], v125 offset:41984
	v_exp_f32_e32 v52, v52
	v_exp_f32_e32 v53, v53
	v_exp_f32_e32 v54, v54
	v_exp_f32_e32 v55, v55
	v_pk_add_f32 v[120:121], v[120:121], v[48:49]
	v_pk_add_f32 v[122:123], v[122:123], v[50:51]
	v_mfma_f32_32x32x64_f8f6f4 v[64:79], v[18:23], v[114:119], v[64:79] cbsz:2 blgp:2
	ds_read_b128 v[18:21], v124 offset:39936
	ds_read_b64 v[22:23], v125 offset:42496
	v_exp_f32_e32 v56, v56
	v_exp_f32_e32 v57, v57
	v_exp_f32_e32 v58, v58
	v_exp_f32_e32 v59, v59
	v_pk_add_f32 v[120:121], v[120:121], v[52:53]
	v_pk_add_f32 v[122:123], v[122:123], v[54:55]
	s_waitcnt lgkmcnt(8)
	v_mfma_f32_32x32x64_f8f6f4 v[80:95], v[24:29], v[96:101], 0 cbsz:2 blgp:2
	ds_read_b128 v[24:27], v124 offset:43008
	ds_read_b64 v[28:29], v125 offset:47104
	v_exp_f32_e32 v60, v60
	v_exp_f32_e32 v61, v61
	v_exp_f32_e32 v62, v62
	v_exp_f32_e32 v63, v63
	v_pk_add_f32 v[120:121], v[120:121], v[56:57]
	v_pk_add_f32 v[122:123], v[122:123], v[58:59]
	v_mfma_f32_32x32x64_f8f6f4 v[80:95], v[30:35], v[102:107], v[80:95] cbsz:2 blgp:2
	ds_read_b128 v[30:33], v124 offset:44032
	ds_read_b64 v[34:35], v125 offset:47616
	v_exp_f32_e32 v64, v64
	v_exp_f32_e32 v65, v65
	v_exp_f32_e32 v66, v66
	v_exp_f32_e32 v67, v67
	v_pk_add_f32 v[120:121], v[120:121], v[60:61]
	v_pk_add_f32 v[122:123], v[122:123], v[62:63]
	v_mfma_f32_32x32x64_f8f6f4 v[80:95], v[36:41], v[108:113], v[80:95] cbsz:2 blgp:2
	ds_read_b128 v[36:39], v124 offset:45056
	ds_read_b64 v[40:41], v125 offset:48128
	v_exp_f32_e32 v68, v68
	v_exp_f32_e32 v69, v69
	v_exp_f32_e32 v70, v70
	v_exp_f32_e32 v71, v71
	v_pk_add_f32 v[120:121], v[120:121], v[64:65]
	v_pk_add_f32 v[122:123], v[122:123], v[66:67]
	v_mfma_f32_32x32x64_f8f6f4 v[80:95], v[42:47], v[114:119], v[80:95] cbsz:2 blgp:2
	ds_read_b128 v[42:45], v124 offset:46080
	ds_read_b64 v[46:47], v125 offset:48640
	v_exp_f32_e32 v72, v72
	v_exp_f32_e32 v73, v73
	v_exp_f32_e32 v74, v74
	v_exp_f32_e32 v75, v75
	v_pk_add_f32 v[120:121], v[120:121], v[68:69]
	v_pk_add_f32 v[122:123], v[122:123], v[70:71]
	s_waitcnt vmcnt(1) lgkmcnt(8)
	v_mfma_f32_32x32x64_f8f6f4 v[48:63], v[0:5], v[96:101], 0 cbsz:2 blgp:2
	s_barrier
	ds_read_b128 v[0:3], v124 offset:49152
	ds_read_b64 v[4:5], v125 offset:53248
	v_exp_f32_e32 v76, v76
	v_exp_f32_e32 v77, v77
	v_exp_f32_e32 v78, v78
	v_exp_f32_e32 v79, v79
	v_pk_add_f32 v[120:121], v[120:121], v[72:73]
	v_pk_add_f32 v[122:123], v[122:123], v[74:75]
	v_mfma_f32_32x32x64_f8f6f4 v[48:63], v[6:11], v[102:107], v[48:63] cbsz:2 blgp:2
	ds_read_b128 v[6:9], v124 offset:50176
	ds_read_b64 v[10:11], v125 offset:53760
	v_exp_f32_e32 v80, v80
	v_exp_f32_e32 v81, v81
	v_exp_f32_e32 v82, v82
	v_exp_f32_e32 v83, v83
	v_pk_add_f32 v[120:121], v[120:121], v[76:77]
	v_pk_add_f32 v[122:123], v[122:123], v[78:79]
	v_mfma_f32_32x32x64_f8f6f4 v[48:63], v[12:17], v[108:113], v[48:63] cbsz:2 blgp:2
	ds_read_b128 v[12:15], v124 offset:51200
	ds_read_b64 v[16:17], v125 offset:54272
	v_exp_f32_e32 v84, v84
	v_exp_f32_e32 v85, v85
	v_exp_f32_e32 v86, v86
	v_exp_f32_e32 v87, v87
	v_pk_add_f32 v[120:121], v[120:121], v[80:81]
	v_pk_add_f32 v[122:123], v[122:123], v[82:83]
	v_mfma_f32_32x32x64_f8f6f4 v[48:63], v[18:23], v[114:119], v[48:63] cbsz:2 blgp:2
	ds_read_b128 v[18:21], v124 offset:52224
	ds_read_b64 v[22:23], v125 offset:54784
	v_exp_f32_e32 v88, v88
	v_exp_f32_e32 v89, v89
	v_exp_f32_e32 v90, v90
	v_exp_f32_e32 v91, v91
	v_pk_add_f32 v[120:121], v[120:121], v[84:85]
	v_pk_add_f32 v[122:123], v[122:123], v[86:87]
	s_waitcnt lgkmcnt(8)
	v_mfma_f32_32x32x64_f8f6f4 v[64:79], v[24:29], v[96:101], 0 cbsz:2 blgp:2
	ds_read_b128 v[24:27], v124 offset:55296
	ds_read_b64 v[28:29], v125 offset:59392
	v_exp_f32_e32 v92, v92
	v_exp_f32_e32 v93, v93
	v_exp_f32_e32 v94, v94
	v_exp_f32_e32 v95, v95
	v_pk_add_f32 v[120:121], v[120:121], v[88:89]
	v_pk_add_f32 v[122:123], v[122:123], v[90:91]
	v_mfma_f32_32x32x64_f8f6f4 v[64:79], v[30:35], v[102:107], v[64:79] cbsz:2 blgp:2
	ds_read_b128 v[30:33], v124 offset:56320
	ds_read_b64 v[34:35], v125 offset:59904
	v_exp_f32_e32 v48, v48
	v_exp_f32_e32 v49, v49
	v_exp_f32_e32 v50, v50
	v_exp_f32_e32 v51, v51
	v_pk_add_f32 v[120:121], v[120:121], v[92:93]
	v_pk_add_f32 v[122:123], v[122:123], v[94:95]
	v_mfma_f32_32x32x64_f8f6f4 v[64:79], v[36:41], v[108:113], v[64:79] cbsz:2 blgp:2
	ds_read_b128 v[36:39], v124 offset:57344
	ds_read_b64 v[40:41], v125 offset:60416
	v_exp_f32_e32 v52, v52
	v_exp_f32_e32 v53, v53
	v_exp_f32_e32 v54, v54
	v_exp_f32_e32 v55, v55
	v_pk_add_f32 v[120:121], v[120:121], v[48:49]
	v_pk_add_f32 v[122:123], v[122:123], v[50:51]
	v_mfma_f32_32x32x64_f8f6f4 v[64:79], v[42:47], v[114:119], v[64:79] cbsz:2 blgp:2
	ds_read_b128 v[42:45], v124 offset:58368
	ds_read_b64 v[46:47], v125 offset:60928
	v_exp_f32_e32 v56, v56
	v_exp_f32_e32 v57, v57
	v_exp_f32_e32 v58, v58
	v_exp_f32_e32 v59, v59
	v_pk_add_f32 v[120:121], v[120:121], v[52:53]
	v_pk_add_f32 v[122:123], v[122:123], v[54:55]
	s_setprio 1
	s_waitcnt vmcnt(0) lgkmcnt(8)
	v_mfma_f32_32x32x64_f8f6f4 v[80:95], v[0:5], v[96:101], 0 cbsz:2 blgp:2
	s_barrier
	ds_read_b128 v[0:3], v124
	ds_read_b64 v[4:5], v125 offset:4096
	v_exp_f32_e32 v60, v60
	v_exp_f32_e32 v61, v61
	v_exp_f32_e32 v62, v62
	v_exp_f32_e32 v63, v63
	v_pk_add_f32 v[120:121], v[120:121], v[56:57]
	v_pk_add_f32 v[122:123], v[122:123], v[58:59]
	v_mfma_f32_32x32x64_f8f6f4 v[80:95], v[6:11], v[102:107], v[80:95] cbsz:2 blgp:2
	ds_read_b128 v[6:9], v124 offset:1024
	ds_read_b64 v[10:11], v125 offset:4608
	v_exp_f32_e32 v64, v64
	v_exp_f32_e32 v65, v65
	v_exp_f32_e32 v66, v66
	v_exp_f32_e32 v67, v67
	v_pk_add_f32 v[120:121], v[120:121], v[60:61]
	v_pk_add_f32 v[122:123], v[122:123], v[62:63]
	v_mfma_f32_32x32x64_f8f6f4 v[80:95], v[12:17], v[108:113], v[80:95] cbsz:2 blgp:2
	ds_read_b128 v[12:15], v124 offset:2048
	ds_read_b64 v[16:17], v125 offset:5120
	v_exp_f32_e32 v68, v68
	v_exp_f32_e32 v69, v69
	v_exp_f32_e32 v70, v70
	v_exp_f32_e32 v71, v71
	v_pk_add_f32 v[120:121], v[120:121], v[64:65]
	v_pk_add_f32 v[122:123], v[122:123], v[66:67]
	v_mfma_f32_32x32x64_f8f6f4 v[80:95], v[18:23], v[114:119], v[80:95] cbsz:2 blgp:2
	ds_read_b128 v[18:21], v124 offset:3072
	ds_read_b64 v[22:23], v125 offset:5632
	v_exp_f32_e32 v72, v72
	v_exp_f32_e32 v73, v73
	v_exp_f32_e32 v74, v74
	v_exp_f32_e32 v75, v75
	v_pk_add_f32 v[120:121], v[120:121], v[68:69]
	v_pk_add_f32 v[122:123], v[122:123], v[70:71]
	s_waitcnt lgkmcnt(8)
	v_mfma_f32_32x32x64_f8f6f4 v[48:63], v[24:29], v[96:101], 0 cbsz:2 blgp:2
	ds_read_b128 v[24:27], v124 offset:6144
	ds_read_b64 v[28:29], v125 offset:10240
	v_exp_f32_e32 v76, v76
	v_exp_f32_e32 v77, v77
	v_exp_f32_e32 v78, v78
	v_exp_f32_e32 v79, v79
	v_pk_add_f32 v[120:121], v[120:121], v[72:73]
	v_pk_add_f32 v[122:123], v[122:123], v[74:75]
	v_mfma_f32_32x32x64_f8f6f4 v[48:63], v[30:35], v[102:107], v[48:63] cbsz:2 blgp:2
	ds_read_b128 v[30:33], v124 offset:7168
	ds_read_b64 v[34:35], v125 offset:10752
	v_exp_f32_e32 v80, v80
	v_exp_f32_e32 v81, v81
	v_exp_f32_e32 v82, v82
	v_exp_f32_e32 v83, v83
	v_pk_add_f32 v[120:121], v[120:121], v[76:77]
	v_pk_add_f32 v[122:123], v[122:123], v[78:79]
	s_cmp_lg_u32 s8, 10
	s_cbranch_scc1 .Lmk_nosplit_b
	v_add_f32_e32 v127, v120, v121
	v_add_f32_e32 v126, v122, v123
	v_mov_b32_e32 v120, 0
	v_mov_b32_e32 v121, 0
	v_mov_b32_e32 v122, 0
	v_mov_b32_e32 v123, 0
	v_add_f32_e32 v127, v127, v126
